# speedup vs baseline: 1.0058x; 1.0005x over previous
_Z12wprep_kernelPKfS0_S0_PDF16_Pj:
	s_load_dwordx8 s[4:11], s[0:1], 0x0
	v_lshl_or_b32 v2, s2, 8, v0
	v_cmp_lt_i32_e32 vcc, 31, v2
	s_and_saveexec_b64 s[2:3], vcc
	s_xor_b64 s[2:3], exec, s[2:3]
	v_mov_b32_e32 v3, 0
	s_andn2_saveexec_b64 s[2:3], s[2:3]
	s_cbranch_execz .LBB0_4
	s_load_dwordx2 s[0:1], s[0:1], 0x20
	v_ashrrev_i32_e32 v3, 31, v2
	v_mov_b32_e32 v1, 0
	s_waitcnt lgkmcnt(0)
	v_lshl_add_u64 v[4:5], v[2:3], 2, s[0:1]
	global_store_dword v[4:5], v1, off sc1
.LBB0_4:
	s_or_b64 exec, exec, s[2:3]
	s_mov_b32 s0, 0x8000
	v_and_b32_e32 v1, 0xffff8000, v2
	s_waitcnt lgkmcnt(0)
	v_mov_b32_e32 v4, s8
	v_mov_b32_e32 v5, s6
	v_cmp_eq_u32_e32 vcc, s0, v1
	s_nop 1
	v_cndmask_b32_e32 v1, v4, v5, vcc
	v_mov_b32_e32 v4, s9
	v_mov_b32_e32 v5, s7
	v_cndmask_b32_e32 v4, v4, v5, vcc
	v_mov_b32_e32 v5, s5
	v_cmp_gt_u32_e32 vcc, s0, v2
	s_nop 1
	v_cndmask_b32_e32 v5, v4, v5, vcc
	v_mov_b32_e32 v4, s4
	v_cndmask_b32_e32 v4, v1, v4, vcc
	v_lshrrev_b32_e32 v1, 4, v0
	v_xor_b32_e32 v6, v1, v0
	v_lshlrev_b32_e32 v0, 9, v2
	v_and_b32_e32 v0, 0xff800, v0
	v_mov_b32_e32 v1, 0
	v_lshl_add_u64 v[4:5], v[4:5], 0, v[0:1]
	v_lshrrev_b32_e32 v0, 4, v2
	v_and_b32_e32 v0, 0x780, v0
	v_lshl_add_u64 v[4:5], v[4:5], 0, v[0:1]
	v_lshlrev_b32_e32 v0, 5, v6
	v_and_b32_e32 v0, 0x60, v0
	v_lshl_add_u64 v[0:1], v[4:5], 0, v[0:1]
	global_load_dwordx4 v[4:7], v[0:1], off nt
	global_load_dwordx4 v[8:11], v[0:1], off offset:16 nt
	v_lshl_add_u64 v[0:1], v[2:3], 4, s[10:11]
	s_waitcnt vmcnt(1)
	v_cvt_pk_f16_f32 v4, v4, v5
	v_cvt_pk_f16_f32 v5, v6, v7
	s_waitcnt vmcnt(0)
	v_cvt_pk_f16_f32 v6, v8, v9
	v_cvt_pk_f16_f32 v7, v10, v11
	global_store_dwordx4 v[0:1], v[4:7], off sc1
	s_endpgm
